# k4_attn_trim
# speedup vs baseline: 1.0084x; 1.0062x over previous
.LBB1_12:
	v_sub_f32_e32 v2, v2, v242
	v_exp_f32_e32 v64, v2
	v_sub_f32_e32 v2, v19, v242
	v_exp_f32_e32 v81, v2
	v_sub_f32_e32 v2, v3, v242
	v_exp_f32_e32 v65, v2
	v_sub_f32_e32 v2, v20, v242
	v_exp_f32_e32 v82, v2
	v_sub_f32_e32 v2, v4, v242
	v_exp_f32_e32 v66, v2
	v_sub_f32_e32 v2, v21, v242
	v_exp_f32_e32 v83, v2
	v_sub_f32_e32 v2, v5, v242
	v_exp_f32_e32 v67, v2
	v_sub_f32_e32 v2, v22, v242
	v_exp_f32_e32 v84, v2
	v_sub_f32_e32 v2, v6, v242
	v_exp_f32_e32 v68, v2
	v_sub_f32_e32 v2, v23, v242
	v_exp_f32_e32 v85, v2
	v_sub_f32_e32 v2, v7, v242
	v_exp_f32_e32 v69, v2
	v_sub_f32_e32 v2, v24, v242
	v_exp_f32_e32 v86, v2
	v_sub_f32_e32 v2, v8, v242
	v_exp_f32_e32 v70, v2
	v_sub_f32_e32 v2, v25, v242
	v_exp_f32_e32 v87, v2
	v_sub_f32_e32 v2, v9, v242
	v_exp_f32_e32 v71, v2
	v_sub_f32_e32 v2, v26, v242
	v_exp_f32_e32 v88, v2
	v_sub_f32_e32 v2, v10, v242
	v_exp_f32_e32 v72, v2
	v_sub_f32_e32 v2, v27, v242
	v_exp_f32_e32 v89, v2
	v_sub_f32_e32 v2, v11, v242
	v_exp_f32_e32 v73, v2
	v_sub_f32_e32 v2, v28, v242
	v_exp_f32_e32 v90, v2
	v_sub_f32_e32 v2, v12, v242
	v_exp_f32_e32 v74, v2
	v_sub_f32_e32 v2, v29, v242
	v_exp_f32_e32 v91, v2
	v_sub_f32_e32 v2, v13, v242
	v_exp_f32_e32 v75, v2
	v_sub_f32_e32 v2, v30, v242
	v_exp_f32_e32 v92, v2
	v_sub_f32_e32 v2, v14, v242
	v_exp_f32_e32 v76, v2
	v_sub_f32_e32 v2, v31, v242
	v_exp_f32_e32 v93, v2
	v_sub_f32_e32 v2, v15, v242
	v_exp_f32_e32 v77, v2
	v_sub_f32_e32 v2, v32, v242
	v_exp_f32_e32 v94, v2
	v_sub_f32_e32 v2, v16, v242
	v_exp_f32_e32 v78, v2
	v_sub_f32_e32 v2, v33, v242
	v_sub_f32_e32 v18, v18, v242
	v_exp_f32_e32 v95, v2
	v_sub_f32_e32 v2, v17, v242
	v_exp_f32_e32 v80, v18
	v_exp_f32_e32 v79, v2
	s_add_i32 s0, s43, 0x80
	s_and_b32 s1, s3, 0x3fffffc0
	v_lshlrev_b32_e32 v2, 1, v0
	v_and_b32_e32 v2, 32, v2
	v_lshlrev_b32_e32 v4, 4, v0
	s_lshr_b32 s40, s0, 6
	s_lshl_b32 s0, s1, 2
	s_lshl_b32 s36, s19, 6
	v_add3_u32 v2, 0, v2, v38
	v_lshlrev_b32_e32 v3, 8, v212
	s_add_i32 s37, s0, 0
	v_and_b32_e32 v4, 0xc0, v4
	s_mov_b32 s14, 1
	v_add3_u32 v240, v2, v3, v4
	s_cmp_lt_u32 s18, 2
	v_add_u32_e32 v202, s4, v1
	v_and_b32_e32 v213, 3, v0
	s_cbranch_scc1 .LBB1_28
	s_lshl_b32 s5, s2, 4
	s_lshl_b32 s4, s42, 7
	s_and_b32 s5, s5, 0x400
	s_lshl_b32 s14, s2, 15
	s_lshr_b32 s16, s3, 2
	s_or_b32 s4, s5, s4
	s_and_b32 s14, s14, 0x400000
	v_mov_b32_e32 v201, 0
	s_and_b32 s16, s16, 0x3ffffff0
	s_mov_b32 s5, 0
	s_add_u32 s16, s6, s16
	v_mov_b32_e32 v203, v201
	s_mov_b32 s15, s5
	s_addc_u32 s17, s7, 0
	v_lshlrev_b64 v[0:1], 11, v[202:203]
	s_add_u32 s16, s16, s14
	v_lshl_add_u64 v[0:1], s[14:15], 0, v[0:1]
	v_lshlrev_b32_e32 v16, 4, v212
	s_addc_u32 s17, s17, 0
	v_lshl_or_b32 v0, v213, 4, v0
	v_mov_b32_e32 v14, v201
	v_mov_b32_e32 v15, v201
	v_lshl_add_u64 v[204:205], s[16:17], 0, v[200:201]
	v_lshl_add_u64 v[206:207], s[8:9], 0, v[0:1]
	s_add_u32 s52, s16, s4
	s_addc_u32 s53, s17, 0
	s_add_u32 s54, s8, s14
	s_addc_u32 s55, s9, s15
	s_add_u32 s54, s54, s4
	s_addc_u32 s55, s55, 0
	v_lshlrev_b32_e32 v250, 11, v202
	v_lshl_or_b32 v250, v213, 4, v250
	v_mov_b32_e32 v0, v201
	v_mov_b32_e32 v1, v201
	v_mov_b32_e32 v2, v201
	v_mov_b32_e32 v3, v201
	v_mov_b32_e32 v4, v201
	v_mov_b32_e32 v5, v201
	v_mov_b32_e32 v6, v201
	v_mov_b32_e32 v7, v201
	v_mov_b32_e32 v8, v201
	v_mov_b32_e32 v9, v201
	v_mov_b32_e32 v10, v201
	v_mov_b32_e32 v11, v201
	v_mov_b32_e32 v12, v201
	v_mov_b32_e32 v13, v201
	v_add_u32_e32 v201, s37, v16
	v_mov_b64_e32 v[30:31], v[14:15]
	v_mov_b64_e32 v[46:47], v[14:15]
	v_cmp_gt_u32_e64 s[0:1], 32, v236
	v_lshl_add_u32 v214, v238, 2, s37
	s_movk_i32 s45, 0x4000
	s_movk_i32 s48, 0x2000
	s_mov_b32 s46, 5
	s_mov_b64 s[14:15], 0x80000
	s_mov_b64 s[16:17], 0x80040
	s_mov_b64 s[18:19], 0x40000
	s_mov_b64 s[20:21], 0x40040
	s_mov_b32 s47, 0x41000000
	s_mov_b64 s[22:23], 0xa0000
	s_mov_b64 s[24:25], 0xa0040
	s_mov_b64 s[26:27], 0x60000
	s_mov_b64 s[28:29], 0x60040
	v_mov_b64_e32 v[28:29], v[12:13]
	v_mov_b64_e32 v[26:27], v[10:11]
	v_mov_b64_e32 v[24:25], v[8:9]
	v_mov_b64_e32 v[22:23], v[6:7]
	v_mov_b64_e32 v[20:21], v[4:5]
	v_mov_b64_e32 v[18:19], v[2:3]
	v_mov_b64_e32 v[16:17], v[0:1]
	v_mov_b64_e32 v[44:45], v[12:13]
	v_mov_b64_e32 v[42:43], v[10:11]
	v_mov_b64_e32 v[40:41], v[8:9]
	v_mov_b64_e32 v[38:39], v[6:7]
	v_mov_b64_e32 v[36:37], v[4:5]
	v_mov_b64_e32 v[34:35], v[2:3]
	v_mov_b64_e32 v[32:33], v[0:1]
	s_mov_b32 s30, s5
.LBB1_14:
	v_add_u32_e32 v203, s30, v240
	ds_read_b64_tr_b16 v[196:197], v203 offset:24576
	ds_read_b64_tr_b16 v[198:199], v203 offset:25088
	s_waitcnt lgkmcnt(9)
	v_mfma_f32_32x32x16_f16 v[112:127], v[192:195], v[148:151], v[48:63]
	v_cvt_pk_f16_f32 v156, v80, v81
	v_cvt_pk_f16_f32 v157, v82, v83
	ds_read_b64_tr_b16 v[192:193], v203 offset:28672
	ds_read_b64_tr_b16 v[194:195], v203 offset:29184
	s_waitcnt lgkmcnt(10)
	v_mfma_f32_32x32x16_f16 v[96:111], v[188:191], v[148:151], v[48:63]
	v_cvt_pk_f16_f32 v158, v84, v85
	v_cvt_pk_f16_f32 v159, v86, v87
	ds_read_b64_tr_b16 v[188:189], v203 offset:25600
	ds_read_b64_tr_b16 v[190:191], v203 offset:26112
	s_waitcnt lgkmcnt(11)
	v_mfma_f32_32x32x16_f16 v[112:127], v[184:187], v[140:143], v[112:127]
	v_cvt_pk_f16_f32 v160, v88, v89
	v_cvt_pk_f16_f32 v161, v90, v91
	ds_read_b64_tr_b16 v[88:89], v203 offset:29696
	ds_read_b64_tr_b16 v[90:91], v203 offset:30208
	s_waitcnt lgkmcnt(12)
	v_mfma_f32_32x32x16_f16 v[96:111], v[176:179], v[140:143], v[96:111]
	v_cvt_pk_f16_f32 v162, v92, v93
	v_cvt_pk_f16_f32 v163, v94, v95
	ds_read_b64_tr_b16 v[84:85], v203 offset:26624
	ds_read_b64_tr_b16 v[86:87], v203 offset:27136
	s_waitcnt lgkmcnt(13)
	v_mfma_f32_32x32x16_f16 v[112:127], v[180:183], v[136:139], v[112:127]
	v_cvt_pk_f16_f32 v152, v64, v65
	v_cvt_pk_f16_f32 v153, v66, v67
	ds_read_b64_tr_b16 v[80:81], v203 offset:30720
	ds_read_b64_tr_b16 v[82:83], v203 offset:31232
	s_waitcnt lgkmcnt(14)
	v_mfma_f32_32x32x16_f16 v[96:111], v[172:175], v[136:139], v[96:111]
	v_cvt_pk_f16_f32 v154, v68, v69
	v_cvt_pk_f16_f32 v155, v70, v71
	ds_read_b64_tr_b16 v[68:69], v203 offset:27648
	ds_read_b64_tr_b16 v[70:71], v203 offset:28160
	s_waitcnt lgkmcnt(14)
	v_mfma_f32_32x32x16_f16 v[112:127], v[168:171], v[132:135], v[112:127]
	v_cvt_pk_f16_f32 v144, v72, v73
	v_cvt_pk_f16_f32 v145, v74, v75
	ds_read_b64_tr_b16 v[64:65], v203 offset:31744
	ds_read_b64_tr_b16 v[66:67], v203 offset:32256
	v_mfma_f32_32x32x16_f16 v[96:111], v[164:167], v[132:135], v[96:111]
	v_cvt_pk_f16_f32 v146, v76, v77
	v_cvt_pk_f16_f32 v147, v78, v79
	s_add_i32 m0, s48, s38
	s_add_u32 s56, s52, 0x80000
	s_addc_u32 s57, s53, 0
	global_load_lds_dwordx4 v200, s[56:57]
	s_add_i32 m0, m0, 0xfc0
	s_add_u32 s58, s54, 0x40000
	s_addc_u32 s59, s55, 0
	global_load_lds_dwordx4 v200, s[56:57] offset:64
	s_add_i32 m0, s45, s39
	s_nop 0
	global_load_lds_dwordx4 v250, s[58:59]
	s_add_i32 m0, m0, 0xfc0
	s_nop 0
	global_load_lds_dwordx4 v250, s[58:59] offset:64
	v_max_f32_e32 v72, v112, v113
	v_max3_f32 v73, v114, v115, v97
	v_max3_f32 v72, v72, v96, v98
	v_max3_f32 v72, v72, v99, v116
	v_max3_f32 v73, v73, v118, v119
	v_max3_f32 v72, v72, v117, v100
	v_max3_f32 v73, v73, v102, v103
	v_max3_f32 v72, v72, v101, v120
	v_max3_f32 v73, v73, v122, v123
	v_max3_f32 v72, v72, v121, v104
	v_max3_f32 v73, v73, v106, v107
	v_max3_f32 v72, v72, v105, v124
	v_max3_f32 v73, v73, v126, v127
	v_max3_f32 v72, v72, v125, v108
	v_max3_f32 v73, v73, v110, v111
	v_max3_f32 v72, v72, v109, v73
	v_mov_b32_e32 v73, v72
	s_nop 1
	v_permlane32_swap_b32_e32 v72, v73
	v_max_f32_e32 v72, v72, v73
	v_cmp_lt_f32_e32 vcc, s47, v72
	s_cmp_lg_u64 vcc, 0
	s_cselect_b64 s[30:31], -1, 0
	s_cbranch_vccnz .LBB1_22

.LBB1_17:
	s_add_i32 s30, s45, 0x2000
	s_cmpk_lg_i32 s45, 0x4000
	s_cselect_b32 s41, s30, 0
	v_add_u32_e32 v203, s48, v240
	ds_read_b64_tr_b16 v[196:197], v203 offset:24576
	ds_read_b64_tr_b16 v[198:199], v203 offset:25088
	s_waitcnt lgkmcnt(9)
	v_mfma_f32_32x32x16_f16 v[80:95], v[72:75], v[148:151], v[48:63]
	v_cvt_pk_f16_f32 v156, v112, v113
	v_cvt_pk_f16_f32 v157, v114, v115
	ds_read_b64_tr_b16 v[192:193], v203 offset:28672
	ds_read_b64_tr_b16 v[194:195], v203 offset:29184
	s_waitcnt lgkmcnt(10)
	v_mfma_f32_32x32x16_f16 v[64:79], v[180:183], v[148:151], v[48:63]
	v_cvt_pk_f16_f32 v158, v116, v117
	v_cvt_pk_f16_f32 v159, v118, v119
	ds_read_b64_tr_b16 v[180:181], v203 offset:25600
	ds_read_b64_tr_b16 v[182:183], v203 offset:26112
	s_waitcnt lgkmcnt(11)
	v_mfma_f32_32x32x16_f16 v[80:95], v[184:187], v[140:143], v[80:95]
	v_cvt_pk_f16_f32 v160, v120, v121
	v_cvt_pk_f16_f32 v161, v122, v123
	ds_read_b64_tr_b16 v[120:121], v203 offset:29696
	ds_read_b64_tr_b16 v[122:123], v203 offset:30208
	s_waitcnt lgkmcnt(12)
	v_mfma_f32_32x32x16_f16 v[64:79], v[168:171], v[140:143], v[64:79]
	v_cvt_pk_f16_f32 v162, v124, v125
	v_cvt_pk_f16_f32 v163, v126, v127
	ds_read_b64_tr_b16 v[116:117], v203 offset:26624
	ds_read_b64_tr_b16 v[118:119], v203 offset:27136
	s_waitcnt lgkmcnt(13)
	v_mfma_f32_32x32x16_f16 v[80:95], v[188:191], v[136:139], v[80:95]
	v_cvt_pk_f16_f32 v152, v96, v97
	v_cvt_pk_f16_f32 v153, v98, v99
	ds_read_b64_tr_b16 v[112:113], v203 offset:30720
	ds_read_b64_tr_b16 v[114:115], v203 offset:31232
	s_waitcnt lgkmcnt(14)
	v_mfma_f32_32x32x16_f16 v[64:79], v[172:175], v[136:139], v[64:79]
	v_cvt_pk_f16_f32 v154, v100, v101
	v_cvt_pk_f16_f32 v155, v102, v103
	ds_read_b64_tr_b16 v[100:101], v203 offset:27648
	ds_read_b64_tr_b16 v[102:103], v203 offset:28160
	s_waitcnt lgkmcnt(14)
	v_mfma_f32_32x32x16_f16 v[80:95], v[176:179], v[132:135], v[80:95]
	v_cvt_pk_f16_f32 v144, v104, v105
	v_cvt_pk_f16_f32 v145, v106, v107
	ds_read_b64_tr_b16 v[96:97], v203 offset:31744
	ds_read_b64_tr_b16 v[98:99], v203 offset:32256
	v_mfma_f32_32x32x16_f16 v[64:79], v[164:167], v[132:135], v[64:79]
	v_cvt_pk_f16_f32 v146, v108, v109
	v_cvt_pk_f16_f32 v147, v110, v111
	s_add_i32 m0, s45, s38
	s_add_u32 s56, s52, 0xa0000
	s_addc_u32 s57, s53, 0
	global_load_lds_dwordx4 v200, s[56:57]
	s_add_i32 m0, m0, 0xfc0
	s_add_u32 s58, s54, 0x60000
	s_addc_u32 s59, s55, 0
	global_load_lds_dwordx4 v200, s[56:57] offset:64
	s_add_i32 m0, s41, s39
	s_nop 0
	global_load_lds_dwordx4 v250, s[58:59]
	s_add_i32 m0, m0, 0xfc0
	s_nop 0
	global_load_lds_dwordx4 v250, s[58:59] offset:64
	v_max_f32_e32 v104, v80, v81
	v_max3_f32 v105, v82, v83, v65
	v_max3_f32 v104, v104, v64, v66
	v_max3_f32 v104, v104, v67, v84
	v_max3_f32 v105, v105, v86, v87
	v_max3_f32 v104, v104, v85, v68
	v_max3_f32 v105, v105, v70, v71
	v_max3_f32 v104, v104, v69, v88
	v_max3_f32 v105, v105, v90, v91
	v_max3_f32 v104, v104, v89, v72
	v_max3_f32 v105, v105, v74, v75
	v_max3_f32 v104, v104, v73, v92
	v_max3_f32 v105, v105, v94, v95
	v_max3_f32 v104, v104, v93, v76
	v_max3_f32 v105, v105, v78, v79
	v_max3_f32 v104, v104, v77, v105
	v_mov_b32_e32 v105, v104
	s_nop 1
	v_permlane32_swap_b32_e32 v104, v105
	v_max_f32_e32 v104, v104, v105
	v_cmp_lt_f32_e32 vcc, s47, v104
	s_cmp_lg_u64 vcc, 0
	s_cselect_b64 s[30:31], -1, 0
	s_cbranch_vccnz .LBB1_25

.LBB1_20:
	s_add_i32 s30, s41, 0x2000
	s_cmpk_lg_i32 s41, 0x4000
	s_cselect_b32 s44, s30, 0
	s_add_i32 s30, s46, 2
	s_add_u32 s52, s52, 0x40000
	s_addc_u32 s53, s53, 0
	s_add_u32 s54, s54, 0x40000
	s_addc_u32 s55, s55, 0
	s_cmp_ge_u32 s30, s40
	s_cbranch_scc1 .LBB1_35
	s_mov_b32 s46, s30
	s_mov_b32 s30, s45
	s_mov_b32 s48, s41
	s_mov_b32 s45, s44
	s_branch .LBB1_14

	.amdhsa_kernel _Z10attn64_fwdPKDF16_S0_S0_PDF16_
		.amdhsa_group_segment_fixed_size 0
		.amdhsa_private_segment_fixed_size 0
		.amdhsa_kernarg_size 32
		.amdhsa_user_sgpr_count 2
		.amdhsa_user_sgpr_dispatch_ptr 0
		.amdhsa_user_sgpr_queue_ptr 0
		.amdhsa_user_sgpr_kernarg_segment_ptr 1
		.amdhsa_user_sgpr_dispatch_id 0
		.amdhsa_user_sgpr_kernarg_preload_length 0
		.amdhsa_user_sgpr_kernarg_preload_offset 0
		.amdhsa_user_sgpr_private_segment_size 0
		.amdhsa_uses_dynamic_stack 0
		.amdhsa_enable_private_segment 0
		.amdhsa_system_sgpr_workgroup_id_x 1
		.amdhsa_system_sgpr_workgroup_id_y 0
		.amdhsa_system_sgpr_workgroup_id_z 0
		.amdhsa_system_sgpr_workgroup_info 0
		.amdhsa_system_vgpr_workitem_id 0
		.amdhsa_next_free_vgpr 252
		.amdhsa_next_free_sgpr 60
		.amdhsa_accum_offset 252
		.amdhsa_reserve_vcc 1
		.amdhsa_float_round_mode_32 0
		.amdhsa_float_round_mode_16_64 0
		.amdhsa_float_denorm_mode_32 3
		.amdhsa_float_denorm_mode_16_64 3
		.amdhsa_dx10_clamp 1
		.amdhsa_ieee_mode 1
		.amdhsa_fp16_overflow 0
		.amdhsa_tg_split 0
		.amdhsa_exception_fp_ieee_invalid_op 0
		.amdhsa_exception_fp_denorm_src 0
		.amdhsa_exception_fp_ieee_div_zero 0
		.amdhsa_exception_fp_ieee_overflow 0
		.amdhsa_exception_fp_ieee_underflow 0
		.amdhsa_exception_fp_ieee_inexact 0
		.amdhsa_exception_int_div_zero 0
	.end_amdhsa_kernel

amdhsa.kernels:
  - .agpr_count:     0
    .args:
      - .address_space:  global
        .offset:         0
        .size:           8
        .value_kind:     global_buffer
      - .address_space:  global
        .offset:         8
        .size:           8
        .value_kind:     global_buffer
      - .address_space:  global
        .offset:         16
        .size:           8
        .value_kind:     global_buffer
      - .address_space:  global
        .offset:         24
        .size:           8
        .value_kind:     global_buffer
      - .address_space:  global
        .offset:         32
        .size:           8
        .value_kind:     global_buffer
      - .actual_access:  write_only
        .address_space:  global
        .offset:         40
        .size:           8
        .value_kind:     global_buffer
      - .actual_access:  write_only
        .address_space:  global
        .offset:         48
        .size:           8
        .value_kind:     global_buffer
      - .actual_access:  write_only
        .address_space:  global
        .offset:         56
        .size:           8
        .value_kind:     global_buffer
      - .actual_access:  write_only
        .address_space:  global
        .offset:         64
        .size:           8
        .value_kind:     global_buffer
    .group_segment_fixed_size: 0
    .kernarg_segment_align: 8
    .kernarg_segment_size: 72
    .language:       OpenCL C
    .language_version:
      - 2
      - 0
    .max_flat_workgroup_size: 256
    .name:           _Z11prep_kernelPKfS0_S0_S0_S0_PDF16_S1_S1_P15HIP_vector_typeIfLj2EE
    .private_segment_fixed_size: 0
    .sgpr_count:     38
    .sgpr_spill_count: 0
    .symbol:         _Z11prep_kernelPKfS0_S0_S0_S0_PDF16_S1_S1_P15HIP_vector_typeIfLj2EE.kd
    .uniform_work_group_size: 1
    .uses_dynamic_stack: false
    .vgpr_count:     44
    .vgpr_spill_count: 0
    .wavefront_size: 64
  - .agpr_count:     0
    .args:
      - .address_space:  global
        .offset:         0
        .size:           8
        .value_kind:     global_buffer
      - .address_space:  global
        .offset:         8
        .size:           8
        .value_kind:     global_buffer
      - .address_space:  global
        .offset:         16
        .size:           8
        .value_kind:     global_buffer
      - .address_space:  global
        .offset:         24
        .size:           8
        .value_kind:     global_buffer
    .group_segment_fixed_size: 0
    .kernarg_segment_align: 8
    .kernarg_segment_size: 32
    .language:       OpenCL C
    .language_version:
      - 2
      - 0
    .max_flat_workgroup_size: 256
    .name:           _Z10attn64_fwdPKDF16_S0_S0_PDF16_
    .private_segment_fixed_size: 0
    .sgpr_count:     66
    .sgpr_spill_count: 0
    .symbol:         _Z10attn64_fwdPKDF16_S0_S0_PDF16_.kd
    .uniform_work_group_size: 1
    .uses_dynamic_stack: false
    .vgpr_count:     252
    .vgpr_spill_count: 0
    .wavefront_size: 64
  - .agpr_count:     0
    .args:
      - .address_space:  global
        .offset:         0
        .size:           8
        .value_kind:     global_buffer
      - .address_space:  global
        .offset:         8
        .size:           8
        .value_kind:     global_buffer
      - .actual_access:  read_only
        .address_space:  global
        .offset:         16
        .size:           8
        .value_kind:     global_buffer
      - .actual_access:  write_only
        .address_space:  global
        .offset:         24
        .size:           8
        .value_kind:     global_buffer
      - .actual_access:  write_only
        .address_space:  global
        .offset:         32
        .size:           8
        .value_kind:     global_buffer
      - .actual_access:  write_only
        .address_space:  global
        .offset:         40
        .size:           8
        .value_kind:     global_buffer
      - .actual_access:  read_only
        .address_space:  global
        .offset:         48
        .size:           8
        .value_kind:     global_buffer
    .group_segment_fixed_size: 0
    .kernarg_segment_align: 8
    .kernarg_segment_size: 56
    .language:       OpenCL C
    .language_version:
      - 2
      - 0
    .max_flat_workgroup_size: 768
    .name:           _Z11gemm_kernelILi0ELi6ELi4ELi5EEvPKDF16_S1_PK15HIP_vector_typeIfLj4EEPDF16_S6_S6_Pf
    .private_segment_fixed_size: 0
    .sgpr_count:     56
    .sgpr_spill_count: 0
    .symbol:         _Z11gemm_kernelILi0ELi6ELi4ELi5EEvPKDF16_S1_PK15HIP_vector_typeIfLj4EEPDF16_S6_S6_Pf.kd
    .uniform_work_group_size: 1
    .uses_dynamic_stack: false
    .vgpr_count:     168
    .vgpr_spill_count: 0
    .wavefront_size: 64
  - .agpr_count:     0
    .args:
      - .address_space:  global
        .offset:         0
        .size:           8
        .value_kind:     global_buffer
      - .address_space:  global
        .offset:         8
        .size:           8
        .value_kind:     global_buffer
      - .actual_access:  read_only
        .address_space:  global
        .offset:         16
        .size:           8
        .value_kind:     global_buffer
      - .actual_access:  read_only
        .address_space:  global
        .offset:         24
        .size:           8
        .value_kind:     global_buffer
      - .actual_access:  read_only
        .address_space:  global
        .offset:         32
        .size:           8
        .value_kind:     global_buffer
      - .actual_access:  read_only
        .address_space:  global
        .offset:         40
        .size:           8
        .value_kind:     global_buffer
      - .actual_access:  write_only
        .address_space:  global
        .offset:         48
        .size:           8
        .value_kind:     global_buffer
    .group_segment_fixed_size: 0
    .kernarg_segment_align: 8
    .kernarg_segment_size: 56
    .language:       OpenCL C
    .language_version:
      - 2
      - 0
    .max_flat_workgroup_size: 768
    .name:           _Z11gemm_kernelILi1ELi4ELi2ELi5EEvPKDF16_S1_PK15HIP_vector_typeIfLj4EEPDF16_S6_S6_Pf
    .private_segment_fixed_size: 0
    .sgpr_count:     38
    .sgpr_spill_count: 0
    .symbol:         _Z11gemm_kernelILi1ELi4ELi2ELi5EEvPKDF16_S1_PK15HIP_vector_typeIfLj4EEPDF16_S6_S6_Pf.kd
    .uniform_work_group_size: 1
    .uses_dynamic_stack: false
    .vgpr_count:     66
    .vgpr_spill_count: 0
    .wavefront_size: 64
